# dense SwiGLU-up GEMM K-loop: L2 software prefetch of a later K-tile (one dword load per 128-byte line, counted waits raised)
# baseline (speedup 1.0000x reference)
_Z6mk_fwd4Args:
	v_readfirstlane_b32 s101, v0
	s_lshr_b32 s101, s101, 6
	s_cmp_ge_u32 s101, 4
	s_cselect_b32 s100, 1, 0
	s_load_dword s96, s[0:1], 0xa8
	s_load_dwordx8 s[52:59], s[0:1], 0x80
	s_load_dwordx16 s[60:75], s[0:1], 0x0
	s_load_dwordx16 s[36:51], s[0:1], 0x40
	v_writelane_b32 v254, s2, 0
	v_lshlrev_b32_e32 v244, 2, v0
	v_add_u32_e32 v1, 0, v244
	v_writelane_b32 v254, s3, 1
	v_readfirstlane_b32 s2, v0
	v_add_u32_e32 v1, 0x21800, v1
	s_mov_b64 s[4:5], 0
	v_writelane_b32 v254, s2, 2
	s_add_u32 s2, s0, 0xa8
	s_addc_u32 s3, s1, 0
	v_writelane_b32 v254, s2, 3
	v_mov_b32_e32 v2, 0
	s_nop 0
	v_writelane_b32 v254, s3, 4
	s_mov_b32 s2, 0
	s_mov_b32 s3, 1
	s_mov_b32 s6, s2
	s_branch .LBB0_2

.LBB0_564:
	v_mbcnt_lo_u32_b32 v252, -1, 0
	v_mbcnt_hi_u32_b32 v252, -1, v252
	v_mov_b32_e32 v253, s101
	v_and_b32_e32 v253, 3, v253
	v_lshl_add_u32 v252, v253, 6, v252
	v_mul_u32_u24_e32 v252, 0x1000, v252
	s_cmp_lt_i32 s90, 8
	s_cselect_b64 s[0:1], -1, 0
	s_cmp_gt_i32 s91, 7
	s_cselect_b64 s[2:3], -1, 0
	s_and_b64 s[0:1], s[0:1], s[2:3]
	s_andn2_b64 vcc, exec, s[0:1]
	s_cbranch_vccnz .LBB0_581
	s_cmpk_gt_i32 s87, 0xabf
	v_readfirstlane_b32 s5, v0
	s_cbranch_scc1 .LBB0_581
	v_lshrrev_b32_e32 v1, 5, v0
	s_waitcnt lgkmcnt(0)
	v_lshrrev_b32_e32 v3, 1, v0
	v_and_b32_e32 v1, 4, v1
	v_bfe_u32 v2, v0, 2, 2
	s_waitcnt vmcnt(6)
	v_and_b32_e32 v13, 24, v3
	s_add_u32 s28, s58, 0x59680000
	v_or3_b32 v1, v1, v2, v13
	v_lshlrev_b32_e32 v2, 4, v0
	s_addc_u32 s29, s59, 0
	v_or_b32_e32 v10, 0x2000, v2
	s_add_u32 s30, s58, 0x2200000
	v_lshrrev_b32_e32 v3, 7, v10
	s_movk_i32 s2, 0x60
	s_addc_u32 s31, s59, 0
	v_and_or_b32 v4, v3, s2, v1
	s_waitcnt vmcnt(5)
	v_bfe_u32 v14, v0, 2, 4
	s_movk_i32 s2, 0x70
	s_ashr_i32 s34, s87, 31
	v_and_or_b32 v3, v3, s2, v14
	s_lshr_b32 s2, s34, 29
	s_add_i32 s2, s87, s2
	s_lshr_b32 s8, s5, 6
	s_ashr_i32 s3, s2, 3
	s_and_b32 s2, s2, -8
	s_lshr_b32 s10, s5, 8
	s_lshl_b32 s33, s8, 10
	s_sub_i32 s2, s87, s2
	s_cmp_lt_i32 s2, 0
	s_movk_i32 s35, 0x159
	s_cselect_b32 s4, s35, 0x158
	s_mul_i32 s2, s2, s4
	s_add_i32 s2, s2, s3
	s_mul_hi_i32 s3, s2, 0x2fa0be83
	s_lshr_b32 s4, s3, 31
	s_ashr_i32 s3, s3, 5
	s_add_i32 s3, s3, s4
	s_lshl_b32 s6, s3, 2
	s_mulk_i32 s3, 0xac
	s_sub_i32 s2, s2, s3
	s_bfe_u32 s3, s2, 0x2001d
	s_add_i32 s3, s2, s3
	s_sext_i32_i16 s4, s3
	s_and_b32 s3, s3, 0xfffc
	s_sub_i32 s2, s2, s3
	s_sext_i32_i16 s2, s2
	v_and_b32_e32 v5, 32, v0
	s_lshr_b32 s4, s4, 2
	s_add_i32 s20, s6, s2
	v_bitop3_b32 v11, v2, v5, 48 bitop3:0x6c
	v_and_b32_e32 v12, 64, v0
	s_ashr_i32 s21, s20, 31
	s_bfe_i64 s[6:7], s[4:5], 0x100000
	v_or_b32_e32 v2, v11, v12
	s_lshl_b64 s[2:3], s[20:21], 20
	s_lshl_b64 s[6:7], s[6:7], 20
	v_lshl_or_b32 v132, v3, 12, v2
	v_lshrrev_b32_e32 v3, 3, v0
	s_add_u32 s24, s30, s6
	v_and_or_b32 v1, v3, 32, v1
	s_addc_u32 s25, s31, s7
	s_add_i32 s21, s33, 0
	v_lshl_or_b32 v134, v1, 12, v2
	s_add_i32 m0, s21, 0x10000
	v_lshl_or_b32 v130, v4, 12, v2
	global_load_lds_dwordx4 v134, s[24:25]
	s_add_i32 m0, s21, 0x12000
	s_add_u32 s6, s24, 0x80000
	global_load_lds_dwordx4 v130, s[24:25]
	s_addc_u32 s7, s25, 0
	s_add_i32 m0, s21, 0x14000
	v_and_or_b32 v1, v3, 48, v14
	global_load_lds_dwordx4 v134, s[6:7]
	s_add_i32 m0, s21, 0x16000
	s_add_u32 s22, s28, s2
	s_addc_u32 s23, s29, s3
	s_add_i32 s36, s21, 0x2000
	v_lshl_or_b32 v136, v1, 12, v2
	global_load_lds_dwordx4 v130, s[6:7]
	s_mov_b32 m0, s21
	s_add_u32 s2, s22, 0x80000
	global_load_lds_dwordx4 v136, s[22:23]
	s_mov_b32 m0, s36
	s_addc_u32 s3, s23, 0
	s_add_i32 s37, s21, 0x4000
	global_load_lds_dwordx4 v132, s[22:23]
	s_mov_b32 m0, s37
	s_add_i32 s42, s21, 0x6000
	global_load_lds_dwordx4 v136, s[2:3]
	s_mov_b32 m0, s42
	v_mov_b32_e32 v135, 0
	global_load_lds_dwordx4 v132, s[2:3]
	v_mov_b32_e32 v131, v135
	v_mov_b32_e32 v137, v135
	v_mov_b32_e32 v133, v135
	s_cmp_eq_u32 s10, 1
	s_mov_b32 s43, 0
	v_lshl_add_u64 v[8:9], s[24:25], 0, v[134:135]
	v_lshl_add_u64 v[6:7], s[24:25], 0, v[130:131]
	v_lshl_add_u64 v[2:3], s[22:23], 0, v[136:137]
	s_cselect_b64 s[2:3], -1, 0
	s_cmp_lg_u32 s10, 1
	v_lshl_add_u64 v[4:5], s[22:23], 0, v[132:133]
	s_cbranch_scc1 .LBB0_568
	s_barrier

.LBB0_574:
	ds_read_b128 v[146:149], v152
	ds_read_b128 v[156:159], v152 offset:1024
	ds_read_b128 v[160:163], v152 offset:2048
	ds_read_b128 v[164:167], v152 offset:3072
	ds_read_b128 v[168:171], v153
	ds_read_b128 v[172:175], v153 offset:1024
	ds_read_b128 v[176:179], v153 offset:2048
	ds_read_b128 v[180:183], v153 offset:3072
	s_add_u32 s24, s22, 0xfff80080
	s_addc_u32 s25, s23, -1
	s_cmp_eq_u32 s69, 28
	s_cselect_b32 s27, s15, s25
	s_cselect_b32 s26, s65, s24
	s_cselect_b32 s25, s13, s68
	s_cselect_b32 s24, s66, s67
	v_lshl_add_u64 v[216:217], s[22:23], 0, v[138:139]
	s_add_i32 m0, s21, 0xc000
	ds_read_b128 v[184:187], v154
	ds_read_b128 v[188:191], v154 offset:1024
	ds_read_b128 v[192:195], v154 offset:2048
	ds_read_b128 v[196:199], v154 offset:3072
	ds_read_b128 v[200:203], v154 offset:4096
	ds_read_b128 v[204:207], v154 offset:5120
	ds_read_b128 v[208:211], v154 offset:6144
	ds_read_b128 v[212:215], v154 offset:7168
	global_load_lds_dwordx4 v[216:217], off
	v_lshl_add_u64 v[216:217], s[22:23], 0, v[140:141]
	s_add_i32 m0, s21, 0xe000
	s_nop 0
	global_load_lds_dwordx4 v[216:217], off
	s_waitcnt vmcnt(8)
	s_waitcnt lgkmcnt(0)
	s_barrier
	s_setprio 1
	s_waitcnt lgkmcnt(0)
	v_mfma_f32_16x16x32_bf16 v[126:129], v[146:149], v[184:187], v[126:129]
	v_mfma_f32_16x16x32_bf16 v[122:125], v[160:163], v[184:187], v[122:125]
	v_mfma_f32_16x16x32_bf16 v[110:113], v[146:149], v[192:195], v[110:113]
	v_mfma_f32_16x16x32_bf16 v[106:109], v[160:163], v[192:195], v[106:109]
	v_mfma_f32_16x16x32_bf16 v[94:97], v[146:149], v[200:203], v[94:97]
	v_mfma_f32_16x16x32_bf16 v[90:93], v[160:163], v[200:203], v[90:93]
	v_mfma_f32_16x16x32_bf16 v[78:81], v[146:149], v[208:211], v[78:81]
	v_mfma_f32_16x16x32_bf16 v[74:77], v[160:163], v[208:211], v[74:77]
	v_mfma_f32_16x16x32_bf16 v[126:129], v[156:159], v[188:191], v[126:129]
	v_mfma_f32_16x16x32_bf16 v[122:125], v[164:167], v[188:191], v[122:125]
	v_mfma_f32_16x16x32_bf16 v[110:113], v[156:159], v[196:199], v[110:113]
	v_mfma_f32_16x16x32_bf16 v[106:109], v[164:167], v[196:199], v[106:109]
	v_mfma_f32_16x16x32_bf16 v[94:97], v[156:159], v[204:207], v[94:97]
	v_mfma_f32_16x16x32_bf16 v[90:93], v[164:167], v[204:207], v[90:93]
	v_mfma_f32_16x16x32_bf16 v[78:81], v[156:159], v[212:215], v[78:81]
	v_mfma_f32_16x16x32_bf16 v[74:77], v[164:167], v[212:215], v[74:77]
	s_setprio 0
	s_setprio 1
	v_mfma_f32_16x16x32_bf16 v[118:121], v[168:171], v[184:187], v[118:121]
	v_mfma_f32_16x16x32_bf16 v[114:117], v[176:179], v[184:187], v[114:117]
	v_mfma_f32_16x16x32_bf16 v[102:105], v[168:171], v[192:195], v[102:105]
	v_mfma_f32_16x16x32_bf16 v[98:101], v[176:179], v[192:195], v[98:101]
	v_mfma_f32_16x16x32_bf16 v[86:89], v[168:171], v[200:203], v[86:89]
	v_mfma_f32_16x16x32_bf16 v[82:85], v[176:179], v[200:203], v[82:85]
	v_mfma_f32_16x16x32_bf16 v[70:73], v[168:171], v[208:211], v[70:73]
	v_mfma_f32_16x16x32_bf16 v[66:69], v[176:179], v[208:211], v[66:69]
	v_mfma_f32_16x16x32_bf16 v[118:121], v[172:175], v[188:191], v[118:121]
	v_mfma_f32_16x16x32_bf16 v[114:117], v[180:183], v[188:191], v[114:117]
	v_mfma_f32_16x16x32_bf16 v[102:105], v[172:175], v[196:199], v[102:105]
	v_mfma_f32_16x16x32_bf16 v[98:101], v[180:183], v[196:199], v[98:101]
	v_mfma_f32_16x16x32_bf16 v[86:89], v[172:175], v[204:207], v[86:89]
	v_mfma_f32_16x16x32_bf16 v[82:85], v[180:183], v[204:207], v[82:85]
	v_mfma_f32_16x16x32_bf16 v[70:73], v[172:175], v[212:215], v[70:73]
	v_mfma_f32_16x16x32_bf16 v[66:69], v[180:183], v[212:215], v[66:69]
	s_setprio 0
	s_barrier
	s_add_i32 s70, s61, s33
	v_lshl_add_u64 v[216:217], s[24:25], 0, v[134:135]
	s_mov_b32 m0, s70
	ds_read_b128 v[184:187], v154 offset:16384
	ds_read_b128 v[188:191], v154 offset:17408
	ds_read_b128 v[192:195], v154 offset:18432
	ds_read_b128 v[196:199], v154 offset:19456
	ds_read_b128 v[200:203], v154 offset:20480
	ds_read_b128 v[204:207], v154 offset:21504
	ds_read_b128 v[208:211], v154 offset:22528
	ds_read_b128 v[212:215], v154 offset:23552
	global_load_lds_dwordx4 v[216:217], off
	s_add_i32 m0, s70, 0x2000
	s_add_u32 s70, s24, 0x80000
	v_lshl_add_u64 v[218:219], s[24:25], 0, v[130:131]
	s_addc_u32 s71, s25, 0
	s_add_i32 s72, s62, s33
	global_load_lds_dwordx4 v[218:219], off
	v_lshl_add_u64 v[220:221], s[70:71], 0, v[134:135]
	s_mov_b32 m0, s72
	v_lshl_add_u64 v[222:223], s[26:27], 0, v[132:133]
	global_load_lds_dwordx4 v[220:221], off
	v_lshl_add_u64 v[220:221], s[70:71], 0, v[130:131]
	s_add_i32 m0, s72, 0x2000
	s_nop 0
	global_load_lds_dwordx4 v[220:221], off
	v_lshl_add_u64 v[220:221], s[26:27], 0, v[136:137]
	s_mov_b32 m0, s21
	s_nop 0
	global_load_lds_dwordx4 v[220:221], off
	s_mov_b32 m0, s36
	s_nop 0
	global_load_lds_dwordx4 v[222:223], off
	s_cmp_lg_u32 s100, 0
	s_cselect_b32 s98, s24, s26
	s_cselect_b32 s99, s25, s27
	global_load_dword v253, v252, s[98:99] offset:256
	global_load_dword v253, v252, s[98:99] offset:384
	s_waitcnt vmcnt(10)
	s_waitcnt lgkmcnt(0)
	s_barrier
	s_setprio 1
	s_waitcnt lgkmcnt(0)
	v_mfma_f32_16x16x32_bf16 v[62:65], v[146:149], v[184:187], v[62:65]
	v_mfma_f32_16x16x32_bf16 v[58:61], v[160:163], v[184:187], v[58:61]
	v_mfma_f32_16x16x32_bf16 v[46:49], v[146:149], v[192:195], v[46:49]
	v_mfma_f32_16x16x32_bf16 v[42:45], v[160:163], v[192:195], v[42:45]
	v_mfma_f32_16x16x32_bf16 v[30:33], v[146:149], v[200:203], v[30:33]
	v_mfma_f32_16x16x32_bf16 v[26:29], v[160:163], v[200:203], v[26:29]
	v_mfma_f32_16x16x32_bf16 v[14:17], v[146:149], v[208:211], v[14:17]
	v_mfma_f32_16x16x32_bf16 v[10:13], v[160:163], v[208:211], v[10:13]
	v_mfma_f32_16x16x32_bf16 v[62:65], v[156:159], v[188:191], v[62:65]
	v_mfma_f32_16x16x32_bf16 v[58:61], v[164:167], v[188:191], v[58:61]
	v_mfma_f32_16x16x32_bf16 v[46:49], v[156:159], v[196:199], v[46:49]
	v_mfma_f32_16x16x32_bf16 v[42:45], v[164:167], v[196:199], v[42:45]
	v_mfma_f32_16x16x32_bf16 v[30:33], v[156:159], v[204:207], v[30:33]
	v_mfma_f32_16x16x32_bf16 v[26:29], v[164:167], v[204:207], v[26:29]
	v_mfma_f32_16x16x32_bf16 v[14:17], v[156:159], v[212:215], v[14:17]
	v_mfma_f32_16x16x32_bf16 v[10:13], v[164:167], v[212:215], v[10:13]
	s_setprio 0
	s_setprio 1
	v_mfma_f32_16x16x32_bf16 v[54:57], v[168:171], v[184:187], v[54:57]
	v_mfma_f32_16x16x32_bf16 v[50:53], v[176:179], v[184:187], v[50:53]
	v_mfma_f32_16x16x32_bf16 v[38:41], v[168:171], v[192:195], v[38:41]
	v_mfma_f32_16x16x32_bf16 v[34:37], v[176:179], v[192:195], v[34:37]
	v_mfma_f32_16x16x32_bf16 v[22:25], v[168:171], v[200:203], v[22:25]
	v_mfma_f32_16x16x32_bf16 v[18:21], v[176:179], v[200:203], v[18:21]
	v_mfma_f32_16x16x32_bf16 v[6:9], v[168:171], v[208:211], v[6:9]
	v_mfma_f32_16x16x32_bf16 v[2:5], v[176:179], v[208:211], v[2:5]
	v_mfma_f32_16x16x32_bf16 v[54:57], v[172:175], v[188:191], v[54:57]
	v_mfma_f32_16x16x32_bf16 v[50:53], v[180:183], v[188:191], v[50:53]
	v_mfma_f32_16x16x32_bf16 v[38:41], v[172:175], v[196:199], v[38:41]
	v_mfma_f32_16x16x32_bf16 v[34:37], v[180:183], v[196:199], v[34:37]
	v_mfma_f32_16x16x32_bf16 v[22:25], v[172:175], v[204:207], v[22:25]
	v_mfma_f32_16x16x32_bf16 v[18:21], v[180:183], v[204:207], v[18:21]
	v_mfma_f32_16x16x32_bf16 v[6:9], v[172:175], v[212:215], v[6:9]
	v_mfma_f32_16x16x32_bf16 v[2:5], v[180:183], v[212:215], v[2:5]
	s_setprio 0
	s_barrier
	s_add_i32 s70, 0, 0x18000
	v_add_u32_e32 v155, s70, v150
	s_add_i32 s71, 0, 0x1c000
	ds_read_b128 v[146:149], v155
	ds_read_b128 v[156:159], v155 offset:1024
	ds_read_b128 v[160:163], v155 offset:2048
	ds_read_b128 v[164:167], v155 offset:3072
	v_add_u32_e32 v155, s71, v150
	ds_read_b128 v[168:171], v155
	ds_read_b128 v[172:175], v155 offset:1024
	ds_read_b128 v[176:179], v155 offset:2048
	ds_read_b128 v[180:183], v155 offset:3072
	s_add_u32 s26, s26, 0x80000
	s_addc_u32 s27, s27, 0
	s_mov_b32 m0, s37
	v_lshl_add_u64 v[224:225], s[26:27], 0, v[136:137]
	ds_read_b128 v[184:187], v154 offset:32768
	ds_read_b128 v[188:191], v154 offset:33792
	ds_read_b128 v[192:195], v154 offset:34816
	ds_read_b128 v[196:199], v154 offset:35840
	ds_read_b128 v[200:203], v154 offset:36864
	ds_read_b128 v[204:207], v154 offset:37888
	ds_read_b128 v[208:211], v154 offset:38912
	ds_read_b128 v[212:215], v154 offset:39936
	global_load_lds_dwordx4 v[224:225], off
	v_lshl_add_u64 v[224:225], s[26:27], 0, v[132:133]
	s_mov_b32 m0, s42
	s_nop 0
	global_load_lds_dwordx4 v[224:225], off
	s_waitcnt vmcnt(10)
	s_waitcnt lgkmcnt(0)
	s_barrier
	s_setprio 1
	s_waitcnt lgkmcnt(0)
	v_mfma_f32_16x16x32_bf16 v[126:129], v[146:149], v[184:187], v[126:129]
	v_mfma_f32_16x16x32_bf16 v[122:125], v[160:163], v[184:187], v[122:125]
	v_mfma_f32_16x16x32_bf16 v[110:113], v[146:149], v[192:195], v[110:113]
	v_mfma_f32_16x16x32_bf16 v[106:109], v[160:163], v[192:195], v[106:109]
	v_mfma_f32_16x16x32_bf16 v[94:97], v[146:149], v[200:203], v[94:97]
	v_mfma_f32_16x16x32_bf16 v[90:93], v[160:163], v[200:203], v[90:93]
	v_mfma_f32_16x16x32_bf16 v[78:81], v[146:149], v[208:211], v[78:81]
	v_mfma_f32_16x16x32_bf16 v[74:77], v[160:163], v[208:211], v[74:77]
	v_mfma_f32_16x16x32_bf16 v[126:129], v[156:159], v[188:191], v[126:129]
	v_mfma_f32_16x16x32_bf16 v[122:125], v[164:167], v[188:191], v[122:125]
	v_mfma_f32_16x16x32_bf16 v[110:113], v[156:159], v[196:199], v[110:113]
	v_mfma_f32_16x16x32_bf16 v[106:109], v[164:167], v[196:199], v[106:109]
	v_mfma_f32_16x16x32_bf16 v[94:97], v[156:159], v[204:207], v[94:97]
	v_mfma_f32_16x16x32_bf16 v[90:93], v[164:167], v[204:207], v[90:93]
	v_mfma_f32_16x16x32_bf16 v[78:81], v[156:159], v[212:215], v[78:81]
	v_mfma_f32_16x16x32_bf16 v[74:77], v[164:167], v[212:215], v[74:77]
	s_setprio 0
	s_setprio 1
	v_mfma_f32_16x16x32_bf16 v[118:121], v[168:171], v[184:187], v[118:121]
	v_mfma_f32_16x16x32_bf16 v[114:117], v[176:179], v[184:187], v[114:117]
	v_mfma_f32_16x16x32_bf16 v[102:105], v[168:171], v[192:195], v[102:105]
	v_mfma_f32_16x16x32_bf16 v[98:101], v[176:179], v[192:195], v[98:101]
	v_mfma_f32_16x16x32_bf16 v[86:89], v[168:171], v[200:203], v[86:89]
	v_mfma_f32_16x16x32_bf16 v[82:85], v[176:179], v[200:203], v[82:85]
	v_mfma_f32_16x16x32_bf16 v[70:73], v[168:171], v[208:211], v[70:73]
	v_mfma_f32_16x16x32_bf16 v[66:69], v[176:179], v[208:211], v[66:69]
	v_mfma_f32_16x16x32_bf16 v[118:121], v[172:175], v[188:191], v[118:121]
	v_mfma_f32_16x16x32_bf16 v[114:117], v[180:183], v[188:191], v[114:117]
	v_mfma_f32_16x16x32_bf16 v[102:105], v[172:175], v[196:199], v[102:105]
	v_mfma_f32_16x16x32_bf16 v[98:101], v[180:183], v[196:199], v[98:101]
	v_mfma_f32_16x16x32_bf16 v[86:89], v[172:175], v[204:207], v[86:89]
	v_mfma_f32_16x16x32_bf16 v[82:85], v[180:183], v[204:207], v[82:85]
	v_mfma_f32_16x16x32_bf16 v[70:73], v[172:175], v[212:215], v[70:73]
	v_mfma_f32_16x16x32_bf16 v[66:69], v[180:183], v[212:215], v[66:69]
	s_setprio 0
	s_barrier
	s_add_i32 s26, s70, s33
	v_lshl_add_u64 v[216:217], v[216:217], 0, s[8:9]
	s_mov_b32 m0, s26
	ds_read_b128 v[184:187], v154 offset:49152
	ds_read_b128 v[188:191], v154 offset:50176
	ds_read_b128 v[192:195], v154 offset:51200
	ds_read_b128 v[196:199], v154 offset:52224
	ds_read_b128 v[200:203], v154 offset:53248
	ds_read_b128 v[204:207], v154 offset:54272
	ds_read_b128 v[208:211], v154 offset:55296
	ds_read_b128 v[212:215], v154 offset:56320
	global_load_lds_dwordx4 v[216:217], off
	s_add_i32 m0, s26, 0x2000
	s_add_u32 s24, s24, 0x80080
	v_lshl_add_u64 v[216:217], v[218:219], 0, s[8:9]
	s_addc_u32 s25, s25, 0
	s_add_i32 s26, s71, s33
	global_load_lds_dwordx4 v[216:217], off
	v_lshl_add_u64 v[216:217], s[24:25], 0, v[134:135]
	s_mov_b32 m0, s26
	s_nop 0
	global_load_lds_dwordx4 v[216:217], off
	v_lshl_add_u64 v[216:217], s[24:25], 0, v[130:131]
	s_add_i32 m0, s26, 0x2000
	s_nop 0
	global_load_lds_dwordx4 v[216:217], off
	v_lshl_add_u64 v[216:217], v[220:221], 0, s[8:9]
	s_mov_b32 m0, s44
	s_nop 0
	global_load_lds_dwordx4 v[216:217], off
	v_lshl_add_u64 v[216:217], v[222:223], 0, s[8:9]
	s_mov_b32 m0, s45
	s_nop 0
	global_load_lds_dwordx4 v[216:217], off
	s_waitcnt vmcnt(10)
	s_waitcnt lgkmcnt(0)
	s_barrier
	s_setprio 1
	s_waitcnt lgkmcnt(0)
	v_mfma_f32_16x16x32_bf16 v[62:65], v[146:149], v[184:187], v[62:65]
	v_mfma_f32_16x16x32_bf16 v[58:61], v[160:163], v[184:187], v[58:61]
	v_mfma_f32_16x16x32_bf16 v[46:49], v[146:149], v[192:195], v[46:49]
	v_mfma_f32_16x16x32_bf16 v[42:45], v[160:163], v[192:195], v[42:45]
	v_mfma_f32_16x16x32_bf16 v[30:33], v[146:149], v[200:203], v[30:33]
	v_mfma_f32_16x16x32_bf16 v[26:29], v[160:163], v[200:203], v[26:29]
	v_mfma_f32_16x16x32_bf16 v[14:17], v[146:149], v[208:211], v[14:17]
	v_mfma_f32_16x16x32_bf16 v[10:13], v[160:163], v[208:211], v[10:13]
	v_mfma_f32_16x16x32_bf16 v[62:65], v[156:159], v[188:191], v[62:65]
	v_mfma_f32_16x16x32_bf16 v[58:61], v[164:167], v[188:191], v[58:61]
	v_mfma_f32_16x16x32_bf16 v[46:49], v[156:159], v[196:199], v[46:49]
	v_mfma_f32_16x16x32_bf16 v[42:45], v[164:167], v[196:199], v[42:45]
	v_mfma_f32_16x16x32_bf16 v[30:33], v[156:159], v[204:207], v[30:33]
	v_mfma_f32_16x16x32_bf16 v[26:29], v[164:167], v[204:207], v[26:29]
	v_mfma_f32_16x16x32_bf16 v[14:17], v[156:159], v[212:215], v[14:17]
	v_mfma_f32_16x16x32_bf16 v[10:13], v[164:167], v[212:215], v[10:13]
	s_setprio 0
	s_setprio 1
	v_mfma_f32_16x16x32_bf16 v[54:57], v[168:171], v[184:187], v[54:57]
	v_mfma_f32_16x16x32_bf16 v[50:53], v[176:179], v[184:187], v[50:53]
	v_mfma_f32_16x16x32_bf16 v[38:41], v[168:171], v[192:195], v[38:41]
	v_mfma_f32_16x16x32_bf16 v[34:37], v[176:179], v[192:195], v[34:37]
	v_mfma_f32_16x16x32_bf16 v[22:25], v[168:171], v[200:203], v[22:25]
	v_mfma_f32_16x16x32_bf16 v[18:21], v[176:179], v[200:203], v[18:21]
	v_mfma_f32_16x16x32_bf16 v[6:9], v[168:171], v[208:211], v[6:9]
	v_mfma_f32_16x16x32_bf16 v[2:5], v[176:179], v[208:211], v[2:5]
	v_mfma_f32_16x16x32_bf16 v[54:57], v[172:175], v[188:191], v[54:57]
	v_mfma_f32_16x16x32_bf16 v[50:53], v[180:183], v[188:191], v[50:53]
	v_mfma_f32_16x16x32_bf16 v[38:41], v[172:175], v[196:199], v[38:41]
	v_mfma_f32_16x16x32_bf16 v[34:37], v[180:183], v[196:199], v[34:37]
	v_mfma_f32_16x16x32_bf16 v[22:25], v[172:175], v[204:207], v[22:25]
	v_mfma_f32_16x16x32_bf16 v[18:21], v[180:183], v[204:207], v[18:21]
	v_mfma_f32_16x16x32_bf16 v[6:9], v[172:175], v[212:215], v[6:9]
	v_mfma_f32_16x16x32_bf16 v[2:5], v[180:183], v[212:215], v[2:5]
	s_setprio 0
	s_barrier
	s_add_i32 s69, s69, 2
	s_add_u32 s22, s22, 0x100
	s_addc_u32 s23, s23, 0
	s_add_u32 s67, s67, 0x100
	s_addc_u32 s68, s68, 0
	s_cmp_gt_u32 s69, 29
	s_cbranch_scc0 .LBB0_574
	s_and_b64 vcc, exec, s[10:11]
	s_cbranch_vccz .LBB0_577
	s_barrier

	.amdhsa_kernel _Z6mk_fwd4Args
		.amdhsa_group_segment_fixed_size 0
		.amdhsa_private_segment_fixed_size 0
		.amdhsa_kernarg_size 424
		.amdhsa_user_sgpr_count 2
		.amdhsa_user_sgpr_dispatch_ptr 0
		.amdhsa_user_sgpr_queue_ptr 0
		.amdhsa_user_sgpr_kernarg_segment_ptr 1
		.amdhsa_user_sgpr_dispatch_id 0
		.amdhsa_user_sgpr_kernarg_preload_length 0
		.amdhsa_user_sgpr_kernarg_preload_offset 0
		.amdhsa_user_sgpr_private_segment_size 0
		.amdhsa_uses_dynamic_stack 0
		.amdhsa_enable_private_segment 0
		.amdhsa_system_sgpr_workgroup_id_x 1
		.amdhsa_system_sgpr_workgroup_id_y 0
		.amdhsa_system_sgpr_workgroup_id_z 0
		.amdhsa_system_sgpr_workgroup_info 0
		.amdhsa_system_vgpr_workitem_id 0
		.amdhsa_next_free_vgpr 256
		.amdhsa_next_free_sgpr 102
		.amdhsa_accum_offset 256
		.amdhsa_reserve_vcc 1
		.amdhsa_float_round_mode_32 0
		.amdhsa_float_round_mode_16_64 0
		.amdhsa_float_denorm_mode_32 3
		.amdhsa_float_denorm_mode_16_64 3
		.amdhsa_dx10_clamp 1
		.amdhsa_ieee_mode 1
		.amdhsa_fp16_overflow 0
		.amdhsa_tg_split 0
		.amdhsa_exception_fp_ieee_invalid_op 0
		.amdhsa_exception_fp_denorm_src 0
		.amdhsa_exception_fp_ieee_div_zero 0
		.amdhsa_exception_fp_ieee_overflow 0
		.amdhsa_exception_fp_ieee_underflow 0
		.amdhsa_exception_fp_ieee_inexact 0
		.amdhsa_exception_int_div_zero 0
	.end_amdhsa_kernel

amdhsa.kernels:
  - .agpr_count:     0
    .args:
      - .offset:         0
        .size:           168
        .value_kind:     by_value
      - .offset:         168
        .size:           4
        .value_kind:     hidden_block_count_x
      - .offset:         172
        .size:           4
        .value_kind:     hidden_block_count_y
      - .offset:         176
        .size:           4
        .value_kind:     hidden_block_count_z
      - .offset:         180
        .size:           2
        .value_kind:     hidden_group_size_x
      - .offset:         182
        .size:           2
        .value_kind:     hidden_group_size_y
      - .offset:         184
        .size:           2
        .value_kind:     hidden_group_size_z
      - .offset:         186
        .size:           2
        .value_kind:     hidden_remainder_x
      - .offset:         188
        .size:           2
        .value_kind:     hidden_remainder_y
      - .offset:         190
        .size:           2
        .value_kind:     hidden_remainder_z
      - .offset:         208
        .size:           8
        .value_kind:     hidden_global_offset_x
      - .offset:         216
        .size:           8
        .value_kind:     hidden_global_offset_y
      - .offset:         224
        .size:           8
        .value_kind:     hidden_global_offset_z
      - .offset:         232
        .size:           2
        .value_kind:     hidden_grid_dims
      - .offset:         288
        .size:           4
        .value_kind:     hidden_dynamic_lds_size
    .group_segment_fixed_size: 0
    .kernarg_segment_align: 8
    .kernarg_segment_size: 424
    .language:       OpenCL C
    .language_version:
      - 2
      - 0
    .max_flat_workgroup_size: 512
    .name:           _Z6mk_fwd4Args
    .private_segment_fixed_size: 0
    .sgpr_count:     108
    .sgpr_spill_count: 108
    .symbol:         _Z6mk_fwd4Args.kd
    .uniform_work_group_size: 1
    .uses_dynamic_stack: false
    .vgpr_count:     256
    .vgpr_spill_count: 0
    .wavefront_size: 64
